# v62 + non-temporal hint on the once-read f32 streams: pconv p rows and the prologue norm's x rows
# speedup vs baseline: 1.0046x; 1.0046x over previous
; __device__ __forceinline__ unsigned pk2(float lo, float hi) { f32x2_cv_ v = {lo, hi}; return __builtin_bit_cast(unsigned, __builtin_convertvector(v, bf16x2_cv_)); }
; __device__ __forceinline__ void phase_norm(Frame& F, const float* hin) {
;     ...
;     for (int row0 = 2 * F.gw(); row0 < T; row0 += 2 * F.ngw()) {
;         f32x4 v[2][4]; float s[2] = {0.f, 0.f};
; #pragma unroll
;         for (int q = 0; q < 2; ++q) { const f32x4* xr = (const f32x4*)(hin + (size_t)(row0 + q) * DM) + F.lane;
; #pragma unroll
;             for (int j = 0; j < 4; ++j) v[q][j] = xr[64 * j]; }
; #pragma unroll
;         for (int q = 0; q < 2; ++q) {
; #pragma unroll
;             for (int j = 0; j < 4; ++j) s[q] += (v[q][j][0] * v[q][j][0] + v[q][j][1] * v[q][j][1]) + (v[q][j][2] * v[q][j][2] + v[q][j][3] * v[q][j][3]);
;             s[q] = wave_sum(s[q]);
;             u32x2* o = (u32x2*)(HB + (size_t)(row0 + q) * DM) + F.lane;
; #pragma unroll
;             for (int j = 0; j < 4; ++j) o[64 * j] = (u32x2){pk2(v[q][j][0], v[q][j][1]), pk2(v[q][j][2], v[q][j][3])};
;             if (F.lane < 16) SSQ[(size_t)(row0 + q) * 16 + F.lane] = F.lane == 0 ? s[q] : 0.f; }
.LBB0_235:
	global_load_dwordx4 v[26:29], v[22:23], off offset:-4096 nt
	global_load_dwordx4 v[30:33], v[22:23], off offset:-3072 nt
	global_load_dwordx4 v[34:37], v[22:23], off offset:-2048 nt
	global_load_dwordx4 v[38:41], v[22:23], off offset:-1024 nt
	global_load_dwordx4 v[14:17], v[22:23], off nt
	global_load_dwordx4 v[10:13], v[22:23], off offset:1024 nt
	global_load_dwordx4 v[6:9], v[22:23], off offset:2048 nt
	global_load_dwordx4 v[2:5], v[22:23], off offset:3072 nt
	v_lshl_add_u64 v[24:25], s[74:75], 0, v[20:21]
	v_add_co_u32_e32 v24, vcc, s3, v24
	s_waitcnt vmcnt(7)
	v_mul_f32_e32 v1, v27, v27
	v_mul_f32_e32 v50, v29, v29
	s_waitcnt vmcnt(6)
	v_mul_f32_e32 v51, v31, v31
	v_mul_f32_e32 v52, v33, v33
	s_waitcnt vmcnt(5)
	v_mul_f32_e32 v53, v35, v35
	v_mul_f32_e32 v54, v37, v37
	v_fmac_f32_e32 v1, v26, v26
	v_fmac_f32_e32 v50, v28, v28
	v_fmac_f32_e32 v51, v30, v30
	v_fmac_f32_e32 v52, v32, v32
	s_waitcnt vmcnt(4)
	v_mul_f32_e32 v55, v39, v39
	v_mul_f32_e32 v56, v41, v41
	v_cvt_pk_bf16_f32 v42, v26, v27
	v_fmac_f32_e32 v53, v34, v34
	v_fmac_f32_e32 v54, v36, v36
	v_add_f32_e32 v1, v1, v50
	v_add_f32_e32 v26, v51, v52
	v_fmac_f32_e32 v55, v38, v38
	v_fmac_f32_e32 v56, v40, v40
	v_add_f32_e32 v27, v53, v54
	v_add_f32_e32 v1, v1, v26
	v_cvt_pk_bf16_f32 v43, v28, v29
	v_add_f32_e32 v28, v55, v56
	v_add_f32_e32 v1, v1, v27
	v_add_f32_e32 v1, v1, v28
	v_addc_co_u32_e32 v25, vcc, 0, v25, vcc
	s_nop 0
	v_add_f32_dpp v1, v1, v1 quad_perm:[1,0,3,2] row_mask:0xf bank_mask:0xf bound_ctrl:1
	v_lshl_add_u64 v[26:27], s[74:75], 0, v[18:19]
	v_cvt_pk_bf16_f32 v44, v30, v31
	v_add_f32_dpp v1, v1, v1 quad_perm:[2,3,0,1] row_mask:0xf bank_mask:0xf bound_ctrl:1
	v_cvt_pk_bf16_f32 v45, v32, v33
	v_cvt_pk_bf16_f32 v46, v34, v35
	v_add_f32_dpp v1, v1, v1 row_half_mirror row_mask:0xf bank_mask:0xf bound_ctrl:1
	v_cvt_pk_bf16_f32 v47, v36, v37
	v_cvt_pk_bf16_f32 v48, v38, v39
	v_add_f32_dpp v1, v1, v1 row_mirror row_mask:0xf bank_mask:0xf bound_ctrl:1
	v_cvt_pk_bf16_f32 v49, v40, v41
	v_readlane_b32 s18, v1, 0
	v_readlane_b32 s20, v1, 16
	v_readlane_b32 s19, v1, 32
	v_readlane_b32 s21, v1, 48
	global_store_dwordx2 v[24:25], v[42:43], off
	global_store_dwordx2 v[24:25], v[44:45], off offset:512
	global_store_dwordx2 v[24:25], v[46:47], off offset:1024
	global_store_dwordx2 v[24:25], v[48:49], off offset:1536
	s_and_saveexec_b64 s[16:17], s[4:5]
	s_cbranch_execz .LBB0_237
	v_mov_b32_e32 v28, s20
	v_mov_b32_e32 v29, s21
	v_pk_add_f32 v[28:29], s[18:19], v[28:29]
	s_nop 0
	v_add_f32_e32 v1, v28, v29
	v_add_co_u32_e32 v28, vcc, 0x26800000, v26
	v_cndmask_b32_e64 v1, 0, v1, s[6:7]
	s_nop 0
	v_addc_co_u32_e32 v29, vcc, 0, v27, vcc
	global_store_dword v[28:29], v1, off

; __device__ __forceinline__ u32x4 pack8(f32x4 a, f32x4 b) { u32x4 w; w.x = pk2(a[0], a[1]); w.y = pk2(a[2], a[3]); w.z = pk2(b[0], b[1]); w.w = pk2(b[2], b[3]); return w; }
; template <class Tp> __device__ __forceinline__ Tp* wsp(const Frame& F, size_t off) { return (Tp*)(F.ws + off); }
; #define PH_BEGIN() do { asm volatile("" : "+v"(F.tid)); F.lane = F.tid & 63; asm volatile("" : "+s"(F.ws)); } while (0)
; #define TPH(id, ...) do { unsigned long long t0_ = 0; if (TPROBE == (id)) t0_ = __builtin_amdgcn_s_memrealtime(); __VA_ARGS__; GRID_BAR(); \
;         if (TPROBE == (id)) { const unsigned long long t1_ = __builtin_amdgcn_s_memrealtime(); while (__builtin_amdgcn_s_memrealtime() - t1_ < 4ull * (t1_ - t0_)) __builtin_amdgcn_s_sleep(8); GRID_BAR(); } } while (0)
; __device__ __forceinline__ void phase_pconv(Frame& F, int l) {
;     const Params& P = *F.P; bf16_t* PB = wsp<bf16_t>(F, WS_PB); const float* pl = P.in[1] + (size_t)l * T * DPLE;
;     for (int i = F.bx * NTHREADS + F.tid; i < T * DPLE / 16; i += F.G * NTHREADS) {
;         const f32x4* pp = (const f32x4*)(pl + (size_t)i * 16); const f32x4 a = pp[0], b2 = pp[1], c2 = pp[2], d2 = pp[3];
;         u32x4* dst = (u32x4*)(PB + (size_t)i * 16); dst[0] = pack8(a, b2); dst[1] = pack8(c2, d2); }
; }
; __global__ void __launch_bounds__(NTHREADS, 2) mega_fwd(Params P) {
;     ...
;         TPH(9, if (l + 1 < NLAYER) { phase_pconv(F, l + 1); PH_BEGIN(); } phase_ple(F, l));
.LBB0_1469:
	s_or_b64 exec, exec, s[44:45]
	s_cmp_eq_u32 s62, 3
	s_waitcnt lgkmcnt(0)
	s_barrier
	s_cbranch_scc1 .LBB0_1474
	v_readlane_b32 s2, v253, 3
	s_nop 1
	v_add_u32_e32 v2, s2, v188
	s_mov_b32 s2, 0x80000
	v_cmp_gt_i32_e32 vcc, s2, v2
	s_and_saveexec_b64 s[10:11], vcc
	v_readlane_b32 s16, v255, 28
	v_readlane_b32 s18, v255, 30
	v_readlane_b32 s6, v255, 26
	v_readlane_b32 s17, v255, 29
	v_readlane_b32 s19, v255, 31
	v_readlane_b32 s7, v255, 27
	s_cbranch_execz .LBB0_1473
	v_ashrrev_i32_e32 v3, 31, v2
	v_lshlrev_b64 v[6:7], 5, v[2:3]
	v_lshl_add_u64 v[6:7], s[74:75], 0, v[6:7]
	s_mov_b64 s[2:3], 0x2ac00010
	v_readlane_b32 s14, v254, 51
	v_lshlrev_b64 v[4:5], 6, v[2:3]
	v_lshl_add_u64 v[6:7], v[6:7], 0, s[2:3]
	s_mov_b64 s[12:13], 0
	v_readlane_b32 s15, v254, 52
	s_cmp_lg_u32 s6, 0x20000
	s_cbranch_scc1 .LBB0_1472
	v_lshl_add_u64 v[20:21], s[14:15], 0, v[4:5]
	global_load_dwordx4 v[24:27], v[20:21], off nt
	global_load_dwordx4 v[28:31], v[20:21], off offset:16 nt
	global_load_dwordx4 v[32:35], v[20:21], off offset:32 nt
	global_load_dwordx4 v[36:39], v[20:21], off offset:48 nt
	s_add_u32 s14, s14, s16
	s_addc_u32 s15, s15, s17
	v_lshl_add_u64 v[20:21], s[14:15], 0, v[4:5]
	global_load_dwordx4 v[40:43], v[20:21], off nt
	global_load_dwordx4 v[44:47], v[20:21], off offset:16 nt
	global_load_dwordx4 v[48:51], v[20:21], off offset:32 nt
	global_load_dwordx4 v[52:55], v[20:21], off offset:48 nt
	s_add_u32 s14, s14, s16
	s_addc_u32 s15, s15, s17
	v_lshl_add_u64 v[20:21], s[14:15], 0, v[4:5]
	global_load_dwordx4 v[56:59], v[20:21], off nt
	global_load_dwordx4 v[60:63], v[20:21], off offset:16 nt
	global_load_dwordx4 v[64:67], v[20:21], off offset:32 nt
	global_load_dwordx4 v[68:71], v[20:21], off offset:48 nt
	s_add_u32 s14, s14, s16
	s_addc_u32 s15, s15, s17
	v_lshl_add_u64 v[20:21], s[14:15], 0, v[4:5]
	global_load_dwordx4 v[72:75], v[20:21], off nt
	global_load_dwordx4 v[76:79], v[20:21], off offset:16 nt
	global_load_dwordx4 v[80:83], v[20:21], off offset:32 nt
	global_load_dwordx4 v[84:87], v[20:21], off offset:48 nt
	s_add_u32 s14, s14, s16
	s_addc_u32 s15, s15, s17
	s_waitcnt vmcnt(12)
	v_cvt_pk_bf16_f32 v8, v24, v25
	v_cvt_pk_bf16_f32 v9, v26, v27
	v_cvt_pk_bf16_f32 v10, v28, v29
	v_cvt_pk_bf16_f32 v11, v30, v31
	v_cvt_pk_bf16_f32 v12, v32, v33
	v_cvt_pk_bf16_f32 v13, v34, v35
	v_cvt_pk_bf16_f32 v14, v36, v37
	v_cvt_pk_bf16_f32 v15, v38, v39
	global_store_dwordx4 v[6:7], v[8:11], off offset:-16
	global_store_dwordx4 v[6:7], v[12:15], off
	s_nop 1
	v_lshl_add_u64 v[6:7], v[6:7], 0, s[18:19]
	s_waitcnt vmcnt(10)
	v_cvt_pk_bf16_f32 v8, v40, v41
	v_cvt_pk_bf16_f32 v9, v42, v43
	v_cvt_pk_bf16_f32 v10, v44, v45
	v_cvt_pk_bf16_f32 v11, v46, v47
	v_cvt_pk_bf16_f32 v12, v48, v49
	v_cvt_pk_bf16_f32 v13, v50, v51
	v_cvt_pk_bf16_f32 v14, v52, v53
	v_cvt_pk_bf16_f32 v15, v54, v55
	global_store_dwordx4 v[6:7], v[8:11], off offset:-16
	global_store_dwordx4 v[6:7], v[12:15], off
	s_nop 1
	v_lshl_add_u64 v[6:7], v[6:7], 0, s[18:19]
	s_waitcnt vmcnt(8)
	v_cvt_pk_bf16_f32 v8, v56, v57
	v_cvt_pk_bf16_f32 v9, v58, v59
	v_cvt_pk_bf16_f32 v10, v60, v61
	v_cvt_pk_bf16_f32 v11, v62, v63
	v_cvt_pk_bf16_f32 v12, v64, v65
	v_cvt_pk_bf16_f32 v13, v66, v67
	v_cvt_pk_bf16_f32 v14, v68, v69
	v_cvt_pk_bf16_f32 v15, v70, v71
	global_store_dwordx4 v[6:7], v[8:11], off offset:-16
	global_store_dwordx4 v[6:7], v[12:15], off
	s_nop 1
	v_lshl_add_u64 v[6:7], v[6:7], 0, s[18:19]
	s_waitcnt vmcnt(6)
	v_cvt_pk_bf16_f32 v8, v72, v73
	v_cvt_pk_bf16_f32 v9, v74, v75
	v_cvt_pk_bf16_f32 v10, v76, v77
	v_cvt_pk_bf16_f32 v11, v78, v79
	v_cvt_pk_bf16_f32 v12, v80, v81
	v_cvt_pk_bf16_f32 v13, v82, v83
	v_cvt_pk_bf16_f32 v14, v84, v85
	v_cvt_pk_bf16_f32 v15, v86, v87
	global_store_dwordx4 v[6:7], v[8:11], off offset:-16
	global_store_dwordx4 v[6:7], v[12:15], off
	s_nop 1
	v_lshl_add_u64 v[6:7], v[6:7], 0, s[18:19]
	s_branch .LBB0_1473
.LBB0_1472:
	s_nop 1
	v_lshl_add_u64 v[20:21], s[14:15], 0, v[4:5]
	global_load_dwordx4 v[8:11], v[20:21], off offset:48 nt
	global_load_dwordx4 v[12:15], v[20:21], off offset:32 nt
	global_load_dwordx4 v[16:19], v[20:21], off offset:16 nt
	s_nop 0
	global_load_dwordx4 v[20:23], v[20:21], off nt
	v_add_u32_e32 v2, s6, v2
	s_add_u32 s14, s14, s16
	s_mov_b32 s2, 0x7ffff
	s_addc_u32 s15, s15, s17
	s_waitcnt vmcnt(0)
	v_cvt_pk_bf16_f32 v12, v12, v13
	v_cvt_pk_bf16_f32 v13, v14, v15
	v_cvt_pk_bf16_f32 v20, v20, v21
	v_cvt_pk_bf16_f32 v21, v22, v23
	v_cvt_pk_bf16_f32 v22, v16, v17
	v_add_co_u32_e32 v16, vcc, -16, v6
	v_cvt_pk_bf16_f32 v14, v8, v9
	s_nop 0
	v_addc_co_u32_e32 v17, vcc, -1, v7, vcc
	v_cvt_pk_bf16_f32 v15, v10, v11
	v_cmp_lt_i32_e32 vcc, s2, v2
	v_cvt_pk_bf16_f32 v23, v18, v19
	flat_store_dwordx4 v[6:7], v[12:15]
	v_lshl_add_u64 v[6:7], v[6:7], 0, s[18:19]
	s_or_b64 s[12:13], vcc, s[12:13]
	flat_store_dwordx4 v[16:17], v[20:23]
	s_andn2_b64 exec, exec, s[12:13]
	s_cbranch_execnz .LBB0_1472
